# grid barrier: early arrivers invalidate only the CU L1 (buffer_inv sc0); each XCD's last arriver keeps wbl2 + agent-scope buffer_inv sc1
# speedup vs baseline: 1.0133x; 1.0047x over previous
; __device__ __forceinline__ unsigned xb_ld(unsigned* p)              { return __hip_atomic_load(p, __ATOMIC_RELAXED, __HIP_MEMORY_SCOPE_AGENT); }
; __device__ __forceinline__ unsigned xb_add(unsigned* p, unsigned v) { return __hip_atomic_fetch_add(p, v, __ATOMIC_RELAXED, __HIP_MEMORY_SCOPE_AGENT); }
; #define XB_SPIN(cond, bar) do { unsigned _sp = 0; while (cond) { __builtin_amdgcn_s_sleep(1); \
;     if ((++_sp & 255u) == 0u) { if (xb_ld(&(bar)[XB_TMO])) break; if (_sp > XB_SPIN_CAP) { atomicAdd(&(bar)[XB_TMO], 1u); break; } } } } while (0)
; __device__ __forceinline__ void xcd_barrier(const XcdBarrier& b) {
;     ...
;     if (b.w0 == 0 && ln_ == 0) {
;         unsigned* bar = b.bar; unsigned one_ = 1u;
;         asm volatile("" : "+s"(bar), "+v"(one_));
;         __builtin_amdgcn_s_waitcnt(0);
;         unsigned nloc = b.st[0], nx = b.st[1];
;         if (nloc == 0u) { xcd_barrier_complete(bar, b.x, nloc, nx); b.st[0] = nloc; b.st[1] = nx; }
;         const unsigned old = xb_add(&bar[XB_XSUB(b.x)], one_);
;         const unsigned gen = old / nloc;
;         if (old + 1u == (gen + 1u) * nloc) {
;             __builtin_amdgcn_fence(__ATOMIC_RELEASE, "agent");
;             asm volatile("s_waitcnt vmcnt(0)" ::: "memory");
;             const unsigned og = xb_add(&bar[XB_TOP], one_);
;             const unsigned tg = og / nx;
;             if (og + 1u == (tg + 1u) * nx) xb_add(&bar[XB_TOPGEN], one_);
;             else XB_SPIN(xb_ld(&bar[XB_TOPGEN]) == tg, bar);
;             __builtin_amdgcn_fence(__ATOMIC_ACQUIRE, "agent");
;             xb_add(&bar[XB_XGEN(b.x)], one_);
;             asm volatile("s_waitcnt vmcnt(0)" ::: "memory");
;         } else {
;             XB_SPIN(xb_ld(&bar[XB_XGEN(b.x)]) == gen, bar);
;             __builtin_amdgcn_fence(__ATOMIC_ACQUIRE, "agent");
;             asm volatile("s_waitcnt vmcnt(0)" ::: "memory");
;         }
.LBB0_142:
	s_lshl_b32 s2, s33, 8
	s_add_u32 s23, s34, s2
	s_addc_u32 s22, s35, 0
	v_mov_b32_e32 v1, s23
	v_add_co_u32_e32 v4, vcc, 0x1000, v1
	v_mov_b32_e32 v1, s22
	s_nop 0
	v_addc_co_u32_e32 v5, vcc, 0, v1, vcc
	flat_atomic_add v1, v[4:5], v10 offset:1024 sc0
	v_cvt_f32_u32_e32 v3, v2
	v_sub_u32_e32 v4, 0, v2
	v_rcp_iflag_f32_e32 v3, v3
	s_nop 0
	v_mul_f32_e32 v3, 0x4f7ffffe, v3
	v_cvt_u32_f32_e32 v3, v3
	v_mul_lo_u32 v4, v4, v3
	v_mul_hi_u32 v4, v3, v4
	v_add_u32_e32 v3, v3, v4
	s_waitcnt vmcnt(0) lgkmcnt(0)
	v_mul_hi_u32 v3, v1, v3
	v_mul_lo_u32 v5, v3, v2
	v_add_u32_e32 v4, 1, v1
	v_sub_u32_e32 v1, v1, v5
	v_add_u32_e32 v6, 1, v3
	v_cmp_ge_u32_e32 vcc, v1, v2
	v_sub_u32_e32 v5, v1, v2
	s_nop 0
	v_cndmask_b32_e32 v3, v3, v6, vcc
	v_cndmask_b32_e32 v1, v1, v5, vcc
	v_add_u32_e32 v5, 1, v3
	v_cmp_ge_u32_e32 vcc, v1, v2
	s_nop 1
	v_cndmask_b32_e32 v1, v3, v5, vcc
	v_mad_u64_u32 v[2:3], s[2:3], v2, v1, v[2:3]
	v_cmp_ne_u32_e32 vcc, v4, v2
	v_mov_b32_e32 v20, 0
	s_cbranch_vccnz .Lxbar0_nl
	buffer_wbl2 sc1
	s_waitcnt vmcnt(0)
	s_sub_u32 s2, s23, s34
	s_lshr_b32 s2, s2, 6
	s_add_u32 s6, s34, 0x2400
	s_addc_u32 s7, s35, 0
	s_add_u32 s6, s6, s2
	s_addc_u32 s7, s7, 0
	global_atomic_add v20, v10, s[6:7]
	buffer_inv sc1
	s_branch .Lxbar0_poll
.Lxbar0_nl:
	buffer_inv sc0

; __device__ __forceinline__ unsigned xb_ld(unsigned* p)              { return __hip_atomic_load(p, __ATOMIC_RELAXED, __HIP_MEMORY_SCOPE_AGENT); }
; __device__ __forceinline__ unsigned xb_add(unsigned* p, unsigned v) { return __hip_atomic_fetch_add(p, v, __ATOMIC_RELAXED, __HIP_MEMORY_SCOPE_AGENT); }
; #define XB_SPIN(cond, bar) do { unsigned _sp = 0; while (cond) { __builtin_amdgcn_s_sleep(1); \
;     if ((++_sp & 255u) == 0u) { if (xb_ld(&(bar)[XB_TMO])) break; if (_sp > XB_SPIN_CAP) { atomicAdd(&(bar)[XB_TMO], 1u); break; } } } } while (0)
; __device__ __forceinline__ void xcd_barrier(const XcdBarrier& b) {
;     ...
;     if (b.w0 == 0 && ln_ == 0) {
;         unsigned* bar = b.bar; unsigned one_ = 1u;
;         asm volatile("" : "+s"(bar), "+v"(one_));
;         __builtin_amdgcn_s_waitcnt(0);
;         unsigned nloc = b.st[0], nx = b.st[1];
;         if (nloc == 0u) { xcd_barrier_complete(bar, b.x, nloc, nx); b.st[0] = nloc; b.st[1] = nx; }
;         const unsigned old = xb_add(&bar[XB_XSUB(b.x)], one_);
;         const unsigned gen = old / nloc;
;         if (old + 1u == (gen + 1u) * nloc) {
;             __builtin_amdgcn_fence(__ATOMIC_RELEASE, "agent");
;             asm volatile("s_waitcnt vmcnt(0)" ::: "memory");
;             const unsigned og = xb_add(&bar[XB_TOP], one_);
;             const unsigned tg = og / nx;
;             if (og + 1u == (tg + 1u) * nx) xb_add(&bar[XB_TOPGEN], one_);
;             else XB_SPIN(xb_ld(&bar[XB_TOPGEN]) == tg, bar);
;             __builtin_amdgcn_fence(__ATOMIC_ACQUIRE, "agent");
;             xb_add(&bar[XB_XGEN(b.x)], one_);
;             asm volatile("s_waitcnt vmcnt(0)" ::: "memory");
;         } else {
;             XB_SPIN(xb_ld(&bar[XB_XGEN(b.x)]) == gen, bar);
;             __builtin_amdgcn_fence(__ATOMIC_ACQUIRE, "agent");
;             asm volatile("s_waitcnt vmcnt(0)" ::: "memory");
;         }
.LBB0_430:
	v_readlane_b32 s4, v253, 57
	s_lshl_b32 s4, s4, 2
	s_add_u32 s25, s2, s4
	s_addc_u32 s24, s3, 0
	v_mov_b32_e32 v3, s25
	v_add_co_u32_e32 v6, vcc, 0x1000, v3
	v_mov_b32_e32 v3, s24
	s_nop 0
	v_addc_co_u32_e32 v7, vcc, 0, v3, vcc
	flat_atomic_add v5, v[6:7], v1 offset:1024 sc0
	v_cvt_f32_u32_e32 v3, v4
	v_sub_u32_e32 v6, 0, v4
	v_rcp_iflag_f32_e32 v3, v3
	s_nop 0
	v_mul_f32_e32 v3, 0x4f7ffffe, v3
	v_cvt_u32_f32_e32 v3, v3
	v_mul_lo_u32 v6, v6, v3
	v_mul_hi_u32 v6, v3, v6
	v_add_u32_e32 v3, v3, v6
	s_waitcnt vmcnt(0) lgkmcnt(0)
	v_mul_hi_u32 v3, v5, v3
	v_mul_lo_u32 v6, v3, v4
	v_sub_u32_e32 v6, v5, v6
	v_cmp_ge_u32_e32 vcc, v6, v4
	v_add_u32_e32 v7, 1, v3
	s_nop 0
	v_cndmask_b32_e32 v3, v3, v7, vcc
	v_sub_u32_e32 v7, v6, v4
	v_cndmask_b32_e32 v6, v6, v7, vcc
	v_cmp_ge_u32_e32 vcc, v6, v4
	v_add_u32_e32 v6, 1, v3
	s_nop 0
	v_cndmask_b32_e32 v3, v3, v6, vcc
	v_add_u32_e32 v6, 1, v5
	v_mad_u64_u32 v[4:5], s[4:5], v4, v3, v[4:5]
	v_cmp_ne_u32_e32 vcc, v6, v4
	v_mov_b32_e32 v20, 0
	s_cbranch_vccnz .Lxbar1_nl
	buffer_wbl2 sc1
	s_waitcnt vmcnt(0)
	s_sub_u32 s4, s25, s2
	s_lshr_b32 s4, s4, 6
	s_add_u32 s8, s2, 0x2400
	s_addc_u32 s9, s3, 0
	s_add_u32 s8, s8, s4
	s_addc_u32 s9, s9, 0
	global_atomic_add v20, v1, s[8:9]
	buffer_inv sc1
	s_branch .Lxbar1_poll

; __device__ __forceinline__ unsigned xb_ld(unsigned* p)              { return __hip_atomic_load(p, __ATOMIC_RELAXED, __HIP_MEMORY_SCOPE_AGENT); }
; __device__ __forceinline__ unsigned xb_add(unsigned* p, unsigned v) { return __hip_atomic_fetch_add(p, v, __ATOMIC_RELAXED, __HIP_MEMORY_SCOPE_AGENT); }
; #define XB_SPIN(cond, bar) do { unsigned _sp = 0; while (cond) { __builtin_amdgcn_s_sleep(1); \
;     if ((++_sp & 255u) == 0u) { if (xb_ld(&(bar)[XB_TMO])) break; if (_sp > XB_SPIN_CAP) { atomicAdd(&(bar)[XB_TMO], 1u); break; } } } } while (0)
; __device__ __forceinline__ void xcd_barrier(const XcdBarrier& b) {
;     ...
;     if (b.w0 == 0 && ln_ == 0) {
;         unsigned* bar = b.bar; unsigned one_ = 1u;
;         asm volatile("" : "+s"(bar), "+v"(one_));
;         __builtin_amdgcn_s_waitcnt(0);
;         unsigned nloc = b.st[0], nx = b.st[1];
;         if (nloc == 0u) { xcd_barrier_complete(bar, b.x, nloc, nx); b.st[0] = nloc; b.st[1] = nx; }
;         const unsigned old = xb_add(&bar[XB_XSUB(b.x)], one_);
;         const unsigned gen = old / nloc;
;         if (old + 1u == (gen + 1u) * nloc) {
;             __builtin_amdgcn_fence(__ATOMIC_RELEASE, "agent");
;             asm volatile("s_waitcnt vmcnt(0)" ::: "memory");
;             const unsigned og = xb_add(&bar[XB_TOP], one_);
;             const unsigned tg = og / nx;
;             if (og + 1u == (tg + 1u) * nx) xb_add(&bar[XB_TOPGEN], one_);
;             else XB_SPIN(xb_ld(&bar[XB_TOPGEN]) == tg, bar);
;             __builtin_amdgcn_fence(__ATOMIC_ACQUIRE, "agent");
;             xb_add(&bar[XB_XGEN(b.x)], one_);
;             asm volatile("s_waitcnt vmcnt(0)" ::: "memory");
;         } else {
;             XB_SPIN(xb_ld(&bar[XB_XGEN(b.x)]) == gen, bar);
;             __builtin_amdgcn_fence(__ATOMIC_ACQUIRE, "agent");
;             asm volatile("s_waitcnt vmcnt(0)" ::: "memory");
;         }
.LBB0_681:
	v_readlane_b32 s6, v253, 57
	s_lshl_b32 s6, s6, 2
	s_add_u32 s27, s4, s6
	s_addc_u32 s26, s5, 0
	v_mov_b32_e32 v3, s27
	v_add_co_u32_e32 v6, vcc, 0x1000, v3
	v_mov_b32_e32 v3, s26
	s_nop 0
	v_addc_co_u32_e32 v7, vcc, 0, v3, vcc
	flat_atomic_add v5, v[6:7], v1 offset:1024 sc0
	v_cvt_f32_u32_e32 v3, v4
	v_sub_u32_e32 v6, 0, v4
	v_rcp_iflag_f32_e32 v3, v3
	s_nop 0
	v_mul_f32_e32 v3, 0x4f7ffffe, v3
	v_cvt_u32_f32_e32 v3, v3
	v_mul_lo_u32 v6, v6, v3
	v_mul_hi_u32 v6, v3, v6
	v_add_u32_e32 v3, v3, v6
	s_waitcnt vmcnt(0) lgkmcnt(0)
	v_mul_hi_u32 v3, v5, v3
	v_mul_lo_u32 v6, v3, v4
	v_sub_u32_e32 v6, v5, v6
	v_cmp_ge_u32_e32 vcc, v6, v4
	v_add_u32_e32 v7, 1, v3
	s_nop 0
	v_cndmask_b32_e32 v3, v3, v7, vcc
	v_sub_u32_e32 v7, v6, v4
	v_cndmask_b32_e32 v6, v6, v7, vcc
	v_cmp_ge_u32_e32 vcc, v6, v4
	v_add_u32_e32 v6, 1, v3
	s_nop 0
	v_cndmask_b32_e32 v3, v3, v6, vcc
	v_add_u32_e32 v6, 1, v5
	v_mad_u64_u32 v[4:5], s[6:7], v4, v3, v[4:5]
	v_cmp_ne_u32_e32 vcc, v6, v4
	v_mov_b32_e32 v20, 0
	s_cbranch_vccnz .Lxbar2_nl
	buffer_wbl2 sc1
	s_waitcnt vmcnt(0)
	s_sub_u32 s6, s27, s4
	s_lshr_b32 s6, s6, 6
	s_add_u32 s10, s4, 0x2400
	s_addc_u32 s11, s5, 0
	s_add_u32 s10, s10, s6
	s_addc_u32 s11, s11, 0
	global_atomic_add v20, v1, s[10:11]
	buffer_inv sc1
	s_branch .Lxbar2_poll

; __device__ __forceinline__ unsigned xb_ld(unsigned* p)              { return __hip_atomic_load(p, __ATOMIC_RELAXED, __HIP_MEMORY_SCOPE_AGENT); }
; __device__ __forceinline__ unsigned xb_add(unsigned* p, unsigned v) { return __hip_atomic_fetch_add(p, v, __ATOMIC_RELAXED, __HIP_MEMORY_SCOPE_AGENT); }
; #define XB_SPIN(cond, bar) do { unsigned _sp = 0; while (cond) { __builtin_amdgcn_s_sleep(1); \
;     if ((++_sp & 255u) == 0u) { if (xb_ld(&(bar)[XB_TMO])) break; if (_sp > XB_SPIN_CAP) { atomicAdd(&(bar)[XB_TMO], 1u); break; } } } } while (0)
; __device__ __forceinline__ void xcd_barrier(const XcdBarrier& b) {
;     ...
;     if (b.w0 == 0 && ln_ == 0) {
;         unsigned* bar = b.bar; unsigned one_ = 1u;
;         asm volatile("" : "+s"(bar), "+v"(one_));
;         __builtin_amdgcn_s_waitcnt(0);
;         unsigned nloc = b.st[0], nx = b.st[1];
;         if (nloc == 0u) { xcd_barrier_complete(bar, b.x, nloc, nx); b.st[0] = nloc; b.st[1] = nx; }
;         const unsigned old = xb_add(&bar[XB_XSUB(b.x)], one_);
;         const unsigned gen = old / nloc;
;         if (old + 1u == (gen + 1u) * nloc) {
;             __builtin_amdgcn_fence(__ATOMIC_RELEASE, "agent");
;             asm volatile("s_waitcnt vmcnt(0)" ::: "memory");
;             const unsigned og = xb_add(&bar[XB_TOP], one_);
;             const unsigned tg = og / nx;
;             if (og + 1u == (tg + 1u) * nx) xb_add(&bar[XB_TOPGEN], one_);
;             else XB_SPIN(xb_ld(&bar[XB_TOPGEN]) == tg, bar);
;             __builtin_amdgcn_fence(__ATOMIC_ACQUIRE, "agent");
;             xb_add(&bar[XB_XGEN(b.x)], one_);
;             asm volatile("s_waitcnt vmcnt(0)" ::: "memory");
;         } else {
;             XB_SPIN(xb_ld(&bar[XB_XGEN(b.x)]) == gen, bar);
;             __builtin_amdgcn_fence(__ATOMIC_ACQUIRE, "agent");
;             asm volatile("s_waitcnt vmcnt(0)" ::: "memory");
;         }
.LBB0_928:
	v_readlane_b32 s6, v253, 57
	s_lshl_b32 s6, s6, 2
	s_add_u32 s29, s4, s6
	s_addc_u32 s28, s5, 0
	v_mov_b32_e32 v3, s29
	v_add_co_u32_e32 v6, vcc, 0x1000, v3
	v_mov_b32_e32 v3, s28
	s_nop 0
	v_addc_co_u32_e32 v7, vcc, 0, v3, vcc
	flat_atomic_add v5, v[6:7], v1 offset:1024 sc0
	v_cvt_f32_u32_e32 v3, v4
	v_sub_u32_e32 v6, 0, v4
	v_rcp_iflag_f32_e32 v3, v3
	s_nop 0
	v_mul_f32_e32 v3, 0x4f7ffffe, v3
	v_cvt_u32_f32_e32 v3, v3
	v_mul_lo_u32 v6, v6, v3
	v_mul_hi_u32 v6, v3, v6
	v_add_u32_e32 v3, v3, v6
	s_waitcnt vmcnt(0) lgkmcnt(0)
	v_mul_hi_u32 v3, v5, v3
	v_mul_lo_u32 v6, v3, v4
	v_sub_u32_e32 v6, v5, v6
	v_cmp_ge_u32_e32 vcc, v6, v4
	v_add_u32_e32 v7, 1, v3
	s_nop 0
	v_cndmask_b32_e32 v3, v3, v7, vcc
	v_sub_u32_e32 v7, v6, v4
	v_cndmask_b32_e32 v6, v6, v7, vcc
	v_cmp_ge_u32_e32 vcc, v6, v4
	v_add_u32_e32 v6, 1, v3
	s_nop 0
	v_cndmask_b32_e32 v3, v3, v6, vcc
	v_add_u32_e32 v6, 1, v5
	v_mad_u64_u32 v[4:5], s[6:7], v4, v3, v[4:5]
	v_cmp_ne_u32_e32 vcc, v6, v4
	v_mov_b32_e32 v20, 0
	s_cbranch_vccnz .Lxbar4_nl
	buffer_wbl2 sc1
	s_waitcnt vmcnt(0)
	s_sub_u32 s6, s29, s4
	s_lshr_b32 s6, s6, 6
	s_add_u32 s10, s4, 0x2400
	s_addc_u32 s11, s5, 0
	s_add_u32 s10, s10, s6
	s_addc_u32 s11, s11, 0
	global_atomic_add v20, v1, s[10:11]
	buffer_inv sc1
	s_branch .Lxbar4_poll

; __device__ __forceinline__ unsigned xb_ld(unsigned* p)              { return __hip_atomic_load(p, __ATOMIC_RELAXED, __HIP_MEMORY_SCOPE_AGENT); }
; __device__ __forceinline__ unsigned xb_add(unsigned* p, unsigned v) { return __hip_atomic_fetch_add(p, v, __ATOMIC_RELAXED, __HIP_MEMORY_SCOPE_AGENT); }
; #define XB_SPIN(cond, bar) do { unsigned _sp = 0; while (cond) { __builtin_amdgcn_s_sleep(1); \
;     if ((++_sp & 255u) == 0u) { if (xb_ld(&(bar)[XB_TMO])) break; if (_sp > XB_SPIN_CAP) { atomicAdd(&(bar)[XB_TMO], 1u); break; } } } } while (0)
; __device__ __forceinline__ void xcd_barrier(const XcdBarrier& b) {
;     ...
;     if (b.w0 == 0 && ln_ == 0) {
;         unsigned* bar = b.bar; unsigned one_ = 1u;
;         asm volatile("" : "+s"(bar), "+v"(one_));
;         __builtin_amdgcn_s_waitcnt(0);
;         unsigned nloc = b.st[0], nx = b.st[1];
;         if (nloc == 0u) { xcd_barrier_complete(bar, b.x, nloc, nx); b.st[0] = nloc; b.st[1] = nx; }
;         const unsigned old = xb_add(&bar[XB_XSUB(b.x)], one_);
;         const unsigned gen = old / nloc;
;         if (old + 1u == (gen + 1u) * nloc) {
;             __builtin_amdgcn_fence(__ATOMIC_RELEASE, "agent");
;             asm volatile("s_waitcnt vmcnt(0)" ::: "memory");
;             const unsigned og = xb_add(&bar[XB_TOP], one_);
;             const unsigned tg = og / nx;
;             if (og + 1u == (tg + 1u) * nx) xb_add(&bar[XB_TOPGEN], one_);
;             else XB_SPIN(xb_ld(&bar[XB_TOPGEN]) == tg, bar);
;             __builtin_amdgcn_fence(__ATOMIC_ACQUIRE, "agent");
;             xb_add(&bar[XB_XGEN(b.x)], one_);
;             asm volatile("s_waitcnt vmcnt(0)" ::: "memory");
;         } else {
;             XB_SPIN(xb_ld(&bar[XB_XGEN(b.x)]) == gen, bar);
;             __builtin_amdgcn_fence(__ATOMIC_ACQUIRE, "agent");
;             asm volatile("s_waitcnt vmcnt(0)" ::: "memory");
;         }
.LBB0_1016:
	v_readlane_b32 s4, v253, 57
	s_lshl_b32 s4, s4, 2
	s_add_u32 s27, s2, s4
	s_addc_u32 s26, s3, 0
	v_mov_b32_e32 v3, s27
	v_add_co_u32_e32 v6, vcc, 0x1000, v3
	v_mov_b32_e32 v3, s26
	s_nop 0
	v_addc_co_u32_e32 v7, vcc, 0, v3, vcc
	flat_atomic_add v5, v[6:7], v1 offset:1024 sc0
	v_cvt_f32_u32_e32 v3, v4
	v_sub_u32_e32 v6, 0, v4
	v_rcp_iflag_f32_e32 v3, v3
	s_nop 0
	v_mul_f32_e32 v3, 0x4f7ffffe, v3
	v_cvt_u32_f32_e32 v3, v3
	v_mul_lo_u32 v6, v6, v3
	v_mul_hi_u32 v6, v3, v6
	v_add_u32_e32 v3, v3, v6
	s_waitcnt vmcnt(0) lgkmcnt(0)
	v_mul_hi_u32 v3, v5, v3
	v_mul_lo_u32 v6, v3, v4
	v_sub_u32_e32 v6, v5, v6
	v_cmp_ge_u32_e32 vcc, v6, v4
	v_add_u32_e32 v7, 1, v3
	s_nop 0
	v_cndmask_b32_e32 v3, v3, v7, vcc
	v_sub_u32_e32 v7, v6, v4
	v_cndmask_b32_e32 v6, v6, v7, vcc
	v_cmp_ge_u32_e32 vcc, v6, v4
	v_add_u32_e32 v6, 1, v3
	s_nop 0
	v_cndmask_b32_e32 v3, v3, v6, vcc
	v_add_u32_e32 v6, 1, v5
	v_mad_u64_u32 v[4:5], s[4:5], v4, v3, v[4:5]
	v_cmp_ne_u32_e32 vcc, v6, v4
	v_mov_b32_e32 v20, 0
	s_cbranch_vccnz .Lxbar5_nl
	buffer_wbl2 sc1
	s_waitcnt vmcnt(0)
	s_sub_u32 s4, s27, s2
	s_lshr_b32 s4, s4, 6
	s_add_u32 s8, s2, 0x2400
	s_addc_u32 s9, s3, 0
	s_add_u32 s8, s8, s4
	s_addc_u32 s9, s9, 0
	global_atomic_add v20, v1, s[8:9]
	buffer_inv sc1
	s_branch .Lxbar5_poll
